# hyena layer-1 hosting + phase J: issue both tokens expert-row loads before waiting
# baseline (speedup 1.0000x reference)
; __device__ __forceinline__ unsigned lane_getu(unsigned v, int src) { return (unsigned)__builtin_amdgcn_ds_bpermute(src << 2, (int)v); }
; __device__ __forceinline__ void phase_combine(Frame& F, int l) {
;     ...
;         while (mask[0] | mask[1]) {
;             f32x4 r[2][4]; bool on[2];
; #pragma unroll
;             for (int q = 0; q < 2; ++q) { on[q] = mask[q] != 0ull; if (on[q]) { const int e = __builtin_ctzll(mask[q]); mask[q] &= mask[q] - 1; const int s = (int)lane_getu((unsigned)sl[q], e);
;                     roww_load_bf16(ye + ((size_t)e * EROWS + (mm[q] >> 12) * CAP + s) * DM, lane, r[q]); } }
; #pragma unroll
;             for (int q = 0; q < 2; ++q) if (on[q]) {
; #pragma unroll
;                 for (int j = 0; j < 4; ++j) y[q][j] += r[q][j]; }
;         }
.LBB0_1966:
	s_cmp_lg_u64 s[8:9], 0
	s_cselect_b64 s[18:19], -1, 0
	s_cmp_eq_u64 s[8:9], 0
	s_cbranch_scc1 .LBB0_1968
	s_add_u32 s16, s8, -1
	s_ff1_i32_b64 s26, s[8:9]
	s_addc_u32 s17, s9, -1
	s_and_b64 s[8:9], s[16:17], s[8:9]
	s_lshl_b32 s16, s26, 2
	v_mov_b32_e32 v6, s16
	ds_bpermute_b32 v6, v6, v96
	s_lshl_b32 s16, s26, 11
	s_add_u32 s16, s16, s22
	s_addc_u32 s17, 0, s23
	s_waitcnt lgkmcnt(0)
	v_ashrrev_i32_e32 v7, 31, v6
	v_lshl_add_u64 v[6:7], s[16:17], 0, v[6:7]
	v_lshlrev_b64 v[6:7], 11, v[6:7]
	v_lshl_add_u64 v[6:7], v[60:61], 0, v[6:7]
	global_load_dwordx4 v[30:33], v[6:7], off offset:16
	global_load_dwordx4 v[14:17], v[6:7], off
.LBB0_1968:
	s_cmp_lg_u64 s[14:15], 0
	s_cselect_b64 s[16:17], -1, 0
	s_cmp_eq_u64 s[14:15], 0
	s_cbranch_scc1 .Lj_wait
	s_add_u32 s26, s14, -1
	s_ff1_i32_b64 s28, s[14:15]
	s_addc_u32 s27, s15, -1
	s_and_b64 s[14:15], s[26:27], s[14:15]
	s_lshl_b32 s26, s28, 2
	v_mov_b32_e32 v2, s26
	ds_bpermute_b32 v2, v2, v1
	s_lshl_b32 s26, s28, 11
	s_add_u32 s26, s26, s24
	s_addc_u32 s27, 0, s25
	s_waitcnt lgkmcnt(0)
	v_ashrrev_i32_e32 v3, 31, v2
	v_lshl_add_u64 v[2:3], s[26:27], 0, v[2:3]
	v_lshlrev_b64 v[2:3], 11, v[2:3]
	v_lshl_add_u64 v[2:3], v[60:61], 0, v[2:3]
	global_load_dwordx4 v[26:29], v[2:3], off offset:16
	global_load_dwordx4 v[10:13], v[2:3], off
.Lj_wait:
	s_waitcnt vmcnt(0)
	s_andn2_b64 vcc, exec, s[18:19]
	s_cbranch_vccnz .Lj_unp1
	v_lshlrev_b32_e32 v22, 16, v30
	v_lshlrev_b32_e32 v6, 16, v14
	v_and_b32_e32 v7, 0xffff0000, v14
	v_lshlrev_b32_e32 v8, 16, v15
	v_and_b32_e32 v9, 0xffff0000, v15
	v_lshlrev_b32_e32 v14, 16, v16
	v_and_b32_e32 v15, 0xffff0000, v16
	v_lshlrev_b32_e32 v16, 16, v17
	v_and_b32_e32 v17, 0xffff0000, v17
	v_and_b32_e32 v23, 0xffff0000, v30
	v_lshlrev_b32_e32 v24, 16, v31
	v_and_b32_e32 v25, 0xffff0000, v31
	v_lshlrev_b32_e32 v30, 16, v32
	v_and_b32_e32 v31, 0xffff0000, v32
	v_lshlrev_b32_e32 v32, 16, v33
	v_and_b32_e32 v33, 0xffff0000, v33
.Lj_unp1:
	s_andn2_b64 vcc, exec, s[16:17]
	s_cbranch_vccnz .LBB0_1970
	v_lshlrev_b32_e32 v18, 16, v26
	v_lshlrev_b32_e32 v2, 16, v10
	v_and_b32_e32 v3, 0xffff0000, v10
	v_lshlrev_b32_e32 v4, 16, v11
	v_and_b32_e32 v5, 0xffff0000, v11
	v_lshlrev_b32_e32 v10, 16, v12
	v_and_b32_e32 v11, 0xffff0000, v12
	v_lshlrev_b32_e32 v12, 16, v13
	v_and_b32_e32 v13, 0xffff0000, v13
	v_and_b32_e32 v19, 0xffff0000, v26
	v_lshlrev_b32_e32 v20, 16, v27
	v_and_b32_e32 v21, 0xffff0000, v27
	v_lshlrev_b32_e32 v26, 16, v28
	v_and_b32_e32 v27, 0xffff0000, v28
	v_lshlrev_b32_e32 v28, 16, v29
	v_and_b32_e32 v29, 0xffff0000, v29
